# nt (non-temporal) hint on the message output stores of the MP iteration kernels
# speedup vs baseline: 1.0098x; 1.0054x over previous
.LBB5_11:
	v_lshl_or_b32 v219, v219, 8, v191
	s_add_i32 m0, s24, s33
	ds_read_b128 v[226:229], v223 offset:0x3000
	s_waitcnt lgkmcnt(6)
	s_waitcnt lgkmcnt(3)
	ds_read_b128 v[230:233], v143 offset:0x3000
	s_waitcnt lgkmcnt(6)
	s_nop 0
	global_load_lds_dwordx4 v219, s[12:13]
	v_exp_f32_e32 v143, v156
	v_exp_f32_e32 v152, v152
	v_mfma_f32_16x16x32_f16 v[180:183], v[6:9], v[160:163], v[180:183]
	v_lshl_or_b32 v156, v207, 8, v191
	v_add_f32_e32 v143, 1.0, v143
	v_rcp_f32_e32 v143, v143
	v_mfma_f32_16x16x32_f16 v[176:179], v[46:49], v[160:163], v[176:179]
	v_add_u32_e32 v207, 0x3000, v225
	v_fma_f32 v143, v143, v148, v144
	v_exp_f32_e32 v148, v157
	v_exp_f32_e32 v143, v143
	v_mfma_f32_16x16x32_f16 v[160:163], v[70:73], v[160:163], v[184:187]
	v_add_f32_e32 v144, 1.0, v152
	v_add_f32_e32 v148, 1.0, v148
	v_rcp_f32_e32 v148, v148
	v_add_f32_e32 v143, 1.0, v143
	v_rcp_f32_e32 v143, v143
	v_mfma_f32_16x16x32_f16 v[180:183], v[50:53], v[164:167], v[180:183]
	v_fma_f32 v145, v148, v149, v145
	v_rcp_f32_e32 v144, v144
	v_exp_f32_e32 v152, v153
	v_mfma_f32_16x16x32_f16 v[176:179], v[18:21], v[164:167], v[176:179]
	v_fma_f32 v143, v143, -2.0, 1.0
	v_fma_f32 v143, -v144, v143, v143
	v_fma_mixlo_f16 v184, v144, v188, v143 op_sel_hi:[0,1,0]
	v_mfma_f32_16x16x32_f16 v[160:163], v[74:77], v[164:167], v[160:163]
	ds_read_b128 v[164:167], v142 offset:0x3000
	v_exp_f32_e32 v142, v145
	v_add_f32_e32 v143, 1.0, v152
	s_waitcnt lgkmcnt(6)
	v_rcp_f32_e32 v186, v143
	v_add_f32_e32 v142, 1.0, v142
	v_rcp_f32_e32 v148, v142
	v_mfma_f32_16x16x32_f16 v[142:145], v[90:93], v[168:171], v[160:163]
	v_fma_f32 v148, v148, -2.0, 1.0
	v_mfma_f32_16x16x32_f16 v[180:183], v[10:13], v[168:171], v[180:183]
	v_fma_f32 v187, -v186, v148, v148
	v_mfma_f32_16x16x32_f16 v[176:179], v[58:61], v[168:171], v[176:179]
	s_add_i32 m0, s34, 0x4000
	s_waitcnt lgkmcnt(3)
	s_waitcnt lgkmcnt(2)
	v_exp_f32_e32 v148, v158
	global_load_lds_dwordx4 v156, s[12:13]
	v_exp_f32_e32 v149, v154
	v_add_f32_e32 v148, 1.0, v148
	v_rcp_f32_e32 v148, v148
	v_mfma_f32_16x16x32_f16 v[160:163], v[14:17], v[172:175], v[180:183]
	s_waitcnt lgkmcnt(1)
	s_waitcnt lgkmcnt(0)
	v_fma_f32 v146, v148, v150, v146
	v_add_f32_e32 v148, 1.0, v149
	v_exp_f32_e32 v146, v146
	v_rcp_f32_e32 v150, v148
	v_exp_f32_e32 v148, v159
	v_mfma_f32_16x16x32_f16 v[168:171], v[22:25], v[172:175], v[176:179]
	v_add_f32_e32 v146, 1.0, v146
	v_rcp_f32_e32 v146, v146
	v_add_f32_e32 v148, 1.0, v148
	v_rcp_f32_e32 v148, v148
	v_mfma_f32_16x16x32_f16 v[172:175], v[86:89], v[172:175], v[130:133]
	v_fma_f32 v146, v146, -2.0, 1.0
	v_fma_mixhi_f16 v184, v186, v188, v187 op_sel:[0,1,0] op_sel_hi:[0,1,0]
	v_fmac_f32_e32 v147, v148, v151
	v_mfma_f32_16x16x32_f16 v[160:163], v[26:29], v[226:229], v[160:163]
	v_exp_f32_e32 v147, v147
	v_mfma_f32_16x16x32_f16 v[156:159], v[78:81], v[226:229], v[172:175]
	s_nop 2
	v_fma_f32 v172, -v150, v146, v146
	v_exp_f32_e32 v146, v155
	v_mfma_f32_16x16x32_f16 v[168:171], v[34:37], v[226:229], v[168:171]
	v_fma_mixlo_f16 v185, v150, v189, v172 op_sel_hi:[0,1,0]
	v_add_f32_e32 v151, 1.0, v146
	v_mfma_f32_16x16x32_f16 v[160:163], v[30:33], v[230:233], v[160:163]
	v_add_f32_e32 v146, 1.0, v147
	v_mfma_f32_16x16x32_f16 v[152:155], v[38:41], v[230:233], v[168:171]
	s_nop 2
	v_rcp_f32_e32 v168, v146
	v_mfma_f32_16x16x32_f16 v[146:149], v[54:57], v[164:167], v[160:163]
	s_nop 2
	v_rcp_f32_e32 v160, v151
	v_mfma_f32_16x16x32_f16 v[156:159], v[82:85], v[230:233], v[156:159]
	v_fma_f32 v161, v168, -2.0, 1.0
	v_mfma_f32_16x16x32_f16 v[150:153], v[62:65], v[164:167], v[152:155]
	s_nop 2
	v_fma_f32 v154, -v160, v161, v161
	v_fma_mixhi_f16 v185, v160, v189, v154 op_sel:[0,1,0] op_sel_hi:[0,1,0]
	v_mfma_f32_16x16x32_f16 v[154:157], v[94:97], v[164:167], v[156:159]
	global_store_dwordx2 v207, v[184:185], s[0:1] nt
	s_add_i32 s27, s27, 1
	s_add_i32 s20, s20, s30
	s_waitcnt lgkmcnt(0)
	s_waitcnt vmcnt(11)
	v_add_u32_e32 v213, s29, v213
	v_add_u32_e32 v215, s31, v215
	v_add_u32_e32 v217, s29, v217
	s_cmp_lt_i32 s2, s9
	v_mov_b32_e32 v207, v221
	v_mov_b32_e32 v219, v222
	s_cbranch_scc0 .LBB5_16
.LBB5_12:
	s_mov_b32 s28, s2
	s_and_b32 s2, s27, 1
	s_waitcnt lgkmcnt(0)
	s_barrier
	s_mul_i32 s33, s2, 0xc000
	v_or_b32_e32 v162, s33, v197
	v_or_b32_e32 v221, s33, v198
	v_or_b32_e32 v230, s33, v199
	s_cmp_eq_u32 s27, 0
	ds_read_b128 v[134:137], v162 offset:0
	ds_read_b128 v[138:141], v162 offset:0x1000
	ds_read_b128 v[158:161], v162 offset:0x2000
	ds_read_b128 v[162:165], v162 offset:0x3000
	ds_read_b128 v[166:169], v221 offset:0
	s_nop 0
	s_waitcnt lgkmcnt(4)
	s_nop 0
	v_mfma_f32_16x16x32_f16 v[170:173], v[98:101], v[134:137], 0
	ds_read_b128 v[174:177], v221 offset:0x1000
	s_waitcnt lgkmcnt(4)
	s_nop 0
	v_mfma_f32_16x16x32_f16 v[178:181], v[98:101], v[138:141], 0
	ds_read_b128 v[182:185], v221 offset:0x2000
	s_waitcnt lgkmcnt(4)
	s_nop 0
	v_mfma_f32_16x16x32_f16 v[186:189], v[98:101], v[158:161], 0
	ds_read_b128 v[222:225], v221 offset:0x3000
	s_waitcnt lgkmcnt(4)
	s_nop 0
	v_mfma_f32_16x16x32_f16 v[226:229], v[98:101], v[162:165], 0
	ds_read_b128 v[134:137], v230 offset:0
	s_waitcnt lgkmcnt(4)
	s_nop 0
	v_mfma_f32_16x16x32_f16 v[166:169], v[110:113], v[166:169], v[170:173]
	ds_read_b128 v[138:141], v230 offset:0x1000
	s_waitcnt lgkmcnt(4)
	s_nop 0
	v_mfma_f32_16x16x32_f16 v[170:173], v[110:113], v[174:177], v[178:181]
	ds_read_b128 v[158:161], v230 offset:0x2000
	s_waitcnt lgkmcnt(4)
	s_nop 0
	v_mfma_f32_16x16x32_f16 v[174:177], v[110:113], v[182:185], v[186:189]
	ds_read_b128 v[162:165], v230 offset:0x3000
	s_waitcnt lgkmcnt(4)
	s_nop 0
	v_mfma_f32_16x16x32_f16 v[178:181], v[110:113], v[222:225], v[226:229]
	s_cbranch_scc1 .LBB5_14
	v_exp_f32_e32 v146, v146
	v_exp_f32_e32 v147, v147
	v_exp_f32_e32 v150, v150
	v_exp_f32_e32 v151, v151
	v_add_f32_e32 v146, 1.0, v146
	v_add_f32_e32 v147, 1.0, v147
	v_rcp_f32_e32 v146, v146
	v_rcp_f32_e32 v147, v147
	v_add_f32_e32 v150, 1.0, v150
	v_fmac_f32_e32 v142, v154, v146
	v_fmac_f32_e32 v143, v155, v147
	v_exp_f32_e32 v146, v142
	v_exp_f32_e32 v147, v143
	v_rcp_f32_e32 v142, v150
	v_cvt_f32_f16_e32 v150, v0
	v_add_f32_e32 v143, 1.0, v146
	v_add_f32_e32 v147, 1.0, v147
	v_rcp_f32_e32 v146, v143
	v_add_f32_e32 v143, 1.0, v151
	v_rcp_f32_e32 v147, v147
	v_cvt_f32_f16_sdwa v151, v0 dst_sel:DWORD dst_unused:UNUSED_PAD src0_sel:WORD_1
	v_exp_f32_e32 v0, v148
	v_rcp_f32_e32 v143, v143
	v_pk_fma_f32 v[146:147], v[146:147], 2.0, 1.0 op_sel_hi:[1,0,0] neg_lo:[1,0,0] neg_hi:[1,0,0]
	v_exp_f32_e32 v148, v152
	v_add_f32_e32 v0, 1.0, v0
	v_pk_fma_f32 v[146:147], v[142:143], v[146:147], v[146:147] neg_lo:[1,0,0] neg_hi:[1,0,0]
	v_rcp_f32_e32 v0, v0
	v_pk_fma_f32 v[142:143], v[142:143], v[150:151], v[146:147]
	v_exp_f32_e32 v146, v149
	v_add_f32_e32 v147, 1.0, v148
	v_fmac_f32_e32 v144, v156, v0
	v_exp_f32_e32 v0, v144
	v_add_f32_e32 v144, 1.0, v146
	v_rcp_f32_e32 v146, v144
	v_rcp_f32_e32 v144, v147
	v_exp_f32_e32 v147, v153
	v_add_f32_e32 v0, 1.0, v0
	v_fmac_f32_e32 v145, v157, v146
	v_exp_f32_e32 v148, v145
	v_rcp_f32_e32 v146, v0
	v_add_f32_e32 v0, 1.0, v147
	v_rcp_f32_e32 v145, v0
	v_add_f32_e32 v0, 1.0, v148
	v_rcp_f32_e32 v147, v0
	v_cvt_f32_f16_sdwa v149, v1 dst_sel:DWORD dst_unused:UNUSED_PAD src0_sel:WORD_1
	v_cvt_f32_f16_e32 v148, v1
	v_cvt_pk_f16_f32 v0, v142, v143
	v_pk_fma_f32 v[142:143], v[146:147], 2.0, 1.0 op_sel_hi:[1,0,0] neg_lo:[1,0,0] neg_hi:[1,0,0]
	s_nop 0
	v_pk_fma_f32 v[142:143], v[144:145], v[142:143], v[142:143] neg_lo:[1,0,0] neg_hi:[1,0,0]
	s_nop 0
	v_pk_fma_f32 v[142:143], v[144:145], v[148:149], v[142:143]
	s_nop 0
	v_cvt_pk_f16_f32 v1, v142, v143
	v_add_u32_e32 v142, v206, v217
	global_store_dwordx2 v142, v[0:1], s[0:1] nt
.LBB5_14:
	v_or_b32_e32 v0, s33, v200
	ds_read_b128 v[142:145], v0 offset:0
	s_waitcnt lgkmcnt(4)
	s_nop 0
	v_mfma_f32_16x16x32_f16 v[134:137], v[114:117], v[134:137], v[166:169]
	ds_read_b128 v[146:149], v0 offset:0x1000
	s_waitcnt lgkmcnt(4)
	s_nop 0
	v_mfma_f32_16x16x32_f16 v[138:141], v[114:117], v[138:141], v[170:173]
	ds_read_b128 v[150:153], v0 offset:0x2000
	s_waitcnt lgkmcnt(4)
	s_nop 0
	v_mfma_f32_16x16x32_f16 v[154:157], v[114:117], v[158:161], v[174:177]
	ds_read_b128 v[158:161], v0 offset:0x3000
	s_waitcnt lgkmcnt(4)
	s_nop 0
	v_mfma_f32_16x16x32_f16 v[162:165], v[114:117], v[162:165], v[178:181]
	ds_read_b128 v[166:169], v205 offset:0
	s_waitcnt lgkmcnt(4)
	s_nop 0
	v_mfma_f32_16x16x32_f16 v[134:137], v[106:109], v[142:145], v[134:137]
	ds_read_b128 v[142:145], v205 offset:0x100
	s_waitcnt lgkmcnt(4)
	s_nop 0
	v_mfma_f32_16x16x32_f16 v[138:141], v[106:109], v[146:149], v[138:141]
	ds_read_b128 v[146:149], v205 offset:0x200
	s_waitcnt lgkmcnt(4)
	s_nop 0
	v_mfma_f32_16x16x32_f16 v[150:153], v[106:109], v[150:153], v[154:157]
	ds_read_b128 v[154:157], v205 offset:0x300
	s_waitcnt lgkmcnt(4)
	s_nop 0
	v_mfma_f32_16x16x32_f16 v[158:161], v[106:109], v[158:161], v[162:165]
	s_waitcnt lgkmcnt(3)
	s_nop 0
	v_mfma_f32_16x16x32_f16 v[134:137], v[102:105], v[166:169], v[134:137]
	s_waitcnt lgkmcnt(2)
	s_nop 0
	v_mfma_f32_16x16x32_f16 v[138:141], v[102:105], v[142:145], v[138:141]
	s_waitcnt lgkmcnt(1)
	s_nop 0
	v_mfma_f32_16x16x32_f16 v[142:145], v[102:105], v[146:149], v[150:153]
	s_waitcnt lgkmcnt(0)
	s_nop 0
	v_mfma_f32_16x16x32_f16 v[146:149], v[102:105], v[154:157], v[158:161]
	s_nop 1
	v_max_i32_e32 v0, 0, v134
	v_max_i32_e32 v134, 0, v135
	v_max_i32_e32 v1, 0, v136
	v_max_i32_e32 v135, 0, v137
	v_cvt_pk_f16_f32 v1, v1, v135
	v_cvt_pk_f16_f32 v0, v0, v134
	v_max_i32_e32 v134, 0, v138
	v_max_i32_e32 v136, 0, v139
	v_max_i32_e32 v135, 0, v140
	v_max_i32_e32 v137, 0, v141
	v_cvt_pk_f16_f32 v135, v135, v137
	v_cvt_pk_f16_f32 v134, v134, v136
	ds_write2st64_b64 v218, v[0:1], v[134:135] offset1:8
	v_max_i32_e32 v0, 0, v142
	v_max_i32_e32 v134, 0, v143
	v_max_i32_e32 v1, 0, v144
	v_max_i32_e32 v135, 0, v145
	v_cvt_pk_f16_f32 v1, v1, v135
	v_cvt_pk_f16_f32 v0, v0, v134
	v_max_i32_e32 v134, 0, v146
	v_max_i32_e32 v136, 0, v147
	v_max_i32_e32 v135, 0, v148
	v_max_i32_e32 v137, 0, v149
	s_lshl_b32 s34, s2, 14
	v_cvt_pk_f16_f32 v135, v135, v137
	v_cvt_pk_f16_f32 v134, v134, v136
	s_or_b32 s34, s34, 0x18000
	ds_write2st64_b64 v218, v[0:1], v[134:135] offset0:16 offset1:24
	v_or_b32_e32 v172, s34, v197
	v_or_b32_e32 v223, s34, v198
	v_or_b32_e32 v143, s34, v199
	v_or_b32_e32 v142, s34, v200
	v_add_u32_e32 v0, s34, v208
	s_xor_b32 s34, s2, 1
	s_waitcnt vmcnt(2) lgkmcnt(0)
	s_barrier
	ds_read_b128 v[134:137], v201 offset:0
	s_mul_i32 s37, s34, 0xc000
	ds_read_b128 v[138:141], v202 offset:0
	ds_read_b128 v[144:147], v203 offset:0
	ds_read_b128 v[148:151], v204 offset:0
	v_add_u32_e32 v1, s37, v209
	ds_read_b128 v[152:155], v1 offset:0
	ds_read_b128 v[156:159], v1 offset:0x4000
	ds_read_b128 v[160:163], v1 offset:0x8000
	ds_read_b128 v[164:167], v1 offset:0x400
	ds_read_b128 v[168:171], v1 offset:0x4400
	ds_read_b128 v[174:177], v1 offset:0x8400
	ds_read_b128 v[178:181], v172 offset:0
	s_waitcnt lgkmcnt(10)
	v_subrev_u32_e32 v186, 56, v215
	v_mfma_f32_16x16x32_f16 v[182:185], v[2:5], v[134:137], v[118:121]
	v_min_u32_e32 v225, s17, v186
	v_add_u32_e32 v224, s20, v216
	v_mov_b32_e32 v230, s16
	v_mfma_f32_16x16x32_f16 v[186:189], v[42:45], v[134:137], v[122:125]
	v_cmp_gt_u32_e32 vcc, s8, v224
	ds_read_b128 v[226:229], v223 offset:0
	s_waitcnt lgkmcnt(10)
	v_mfma_f32_16x16x32_f16 v[134:137], v[66:69], v[134:137], v[126:129]
	v_lshl_or_b32 v173, v196, 8, v190
	v_cndmask_b32_e32 v230, v230, v224, vcc
	v_lshlrev_b32_e32 v234, 5, v230
	v_mfma_f32_16x16x32_f16 v[182:185], v[6:9], v[138:141], v[182:185]
	v_add_u32_e32 v196, -8, v215
	v_min_u32_e32 v238, s17, v196
	v_subrev_u32_e32 v196, 52, v215
	v_mfma_f32_16x16x32_f16 v[186:189], v[46:49], v[138:141], v[186:189]
	v_add_u32_e32 v221, -4, v215
	v_min_u32_e32 v196, s18, v196
	v_min_u32_e32 v221, s18, v221
	v_mfma_f32_16x16x32_f16 v[230:233], v[70:73], v[138:141], v[134:137]
	global_load_dwordx4 v[134:137], v234, s[6:7]
	global_load_dwordx4 v[138:141], v234, s[6:7] offset:16
	ds_read_b128 v[234:237], v143 offset:0
	s_waitcnt lgkmcnt(10)
	v_lshl_or_b32 v242, v192, 8, v190
	v_mfma_f32_16x16x32_f16 v[182:185], v[50:53], v[144:147], v[182:185]
	global_load_dword v192, v196, s[4:5]
	v_subrev_u32_e32 v239, 48, v215
	global_load_dword v221, v221, s[4:5]
	v_mfma_f32_16x16x32_f16 v[186:189], v[18:21], v[144:147], v[186:189]
	v_min_u32_e32 v222, s19, v215
	v_min_u32_e32 v239, s19, v239
	v_lshl_or_b32 v241, v194, 8, v191
	v_mfma_f32_16x16x32_f16 v[144:147], v[74:77], v[144:147], v[230:233]
	global_load_dword v196, v239, s[4:5]
	ds_read_b128 v[230:233], v142 offset:0
	s_waitcnt lgkmcnt(10)
	global_load_dword v194, v222, s[4:5]
	s_add_i32 s2, s28, s3
	v_mfma_f32_16x16x32_f16 v[182:185], v[10:13], v[148:151], v[182:185]
	v_lshl_or_b32 v243, v193, 8, v190
	global_load_dword v193, v225, s[4:5]
	s_min_i32 s35, s2, s14
	v_mfma_f32_16x16x32_f16 v[186:189], v[58:61], v[148:151], v[186:189]
	global_load_dword v222, v238, s[4:5]
	s_lshl_b32 s35, s35, 14
	s_lshl_b32 s34, s34, 14
	v_mfma_f32_16x16x32_f16 v[148:151], v[90:93], v[148:151], v[144:147]
	s_add_i32 s36, s33, 0
	v_add_u32_e32 v1, s35, v210
	s_add_i32 s38, s25, s34
	s_add_i32 s39, s36, s21
	s_add_i32 s40, s26, s34
	s_add_i32 s34, s36, s23
	s_add_i32 m0, s39, 0x8000
	v_add_u32_e32 v240, s35, v211
	s_add_i32 s41, s34, 0x8000
	s_add_i32 s35, s39, 0x4000
	s_add_i32 s36, s22, s33
	v_add_u32_e32 v239, s37, v212
	ds_read_b128 v[144:147], v201 offset:0x1000
	s_waitcnt lgkmcnt(4)
	s_waitcnt lgkmcnt(5)
	s_nop 0
	v_pk_add_f16 v152, v152, v156
	v_pk_add_f16 v153, v153, v157
	v_pk_add_f16 v154, v154, v158
	v_pk_add_f16 v155, v155, v159
	v_pk_add_f16 v154, v154, v162
	v_pk_add_f16 v155, v155, v163
	v_pk_add_f16 v153, v153, v161
	v_pk_add_f16 v152, v152, v160
	ds_write_b128 v239, v[152:155]
	v_pk_add_f16 v152, v164, v168
	v_pk_add_f16 v153, v165, v169
	v_pk_add_f16 v154, v166, v170
	v_pk_add_f16 v155, v167, v171
	v_pk_add_f16 v154, v154, v176
	v_pk_add_f16 v155, v155, v177
	v_pk_add_f16 v153, v153, v175
	v_pk_add_f16 v152, v152, v174
	ds_write_b128 v239, v[152:155] offset:1024
	ds_read_b128 v[152:155], v202 offset:0x1000
	s_waitcnt lgkmcnt(4)
	global_load_lds_dwordx4 v173, s[12:13]
	s_mov_b32 m0, s38
	ds_read_b128 v[168:171], v203 offset:0x1000
	s_waitcnt lgkmcnt(4)
	v_mfma_f32_16x16x32_f16 v[182:185], v[14:17], v[178:181], v[182:185]
	global_load_lds_dwordx4 v1, s[12:13]
	ds_read_b128 v[174:177], v204 offset:0x1000
	v_mfma_f32_16x16x32_f16 v[186:189], v[22:25], v[178:181], v[186:189]
	s_waitcnt lgkmcnt(4)
	v_mfma_f32_16x16x32_f16 v[178:181], v[86:89], v[178:181], v[130:133]
	v_mfma_f32_16x16x32_f16 v[156:159], v[26:29], v[226:229], v[182:185]
	v_mfma_f32_16x16x32_f16 v[160:163], v[34:37], v[226:229], v[186:189]
	v_mfma_f32_16x16x32_f16 v[164:167], v[78:81], v[226:229], v[178:181]
	v_mfma_f32_16x16x32_f16 v[156:159], v[30:33], v[234:237], v[156:159]
	v_mfma_f32_16x16x32_f16 v[160:163], v[38:41], v[234:237], v[160:163]
	v_mfma_f32_16x16x32_f16 v[164:167], v[82:85], v[234:237], v[164:167]
	v_mfma_f32_16x16x32_f16 v[156:159], v[54:57], v[230:233], v[156:159]
	v_mfma_f32_16x16x32_f16 v[160:163], v[62:65], v[230:233], v[160:163]
	v_mfma_f32_16x16x32_f16 v[164:167], v[94:97], v[230:233], v[164:167]
	s_mov_b32 m0, s41
	ds_read_b64 v[234:235], v0 offset:0
	ds_read_b128 v[178:181], v172 offset:0x1000
	s_waitcnt lgkmcnt(5)
	ds_read_b128 v[186:189], v223 offset:0x1000
	s_waitcnt lgkmcnt(5)
	s_nop 4
	v_exp_f32_e32 v1, v156
	s_waitcnt lgkmcnt(2)
	ds_read_b128 v[230:233], v143 offset:0x1000
	s_waitcnt lgkmcnt(5)
	global_load_lds_dwordx4 v241, s[12:13]
	v_add_f32_e32 v1, 1.0, v1
	v_rcp_f32_e32 v1, v1
	v_exp_f32_e32 v156, v160
	v_mfma_f32_16x16x32_f16 v[182:185], v[2:5], v[144:147], v[118:121]
	v_add_u32_e32 v225, v206, v213
	v_fma_f32 v1, v1, v164, v148
	v_exp_f32_e32 v1, v1
	v_add_f32_e32 v148, 1.0, v156
	v_exp_f32_e32 v156, v157
	v_rcp_f32_e32 v148, v148
	v_add_f32_e32 v1, 1.0, v1
	v_rcp_f32_e32 v1, v1
	v_add_f32_e32 v156, 1.0, v156
	v_rcp_f32_e32 v156, v156
	v_mfma_f32_16x16x32_f16 v[226:229], v[42:45], v[144:147], v[122:125]
	v_fma_f32 v1, v1, -2.0, 1.0
	v_fma_f32 v1, -v148, v1, v1
	v_fma_mixlo_f16 v1, v148, v234, v1 op_sel_hi:[0,1,0]
	v_mfma_f32_16x16x32_f16 v[144:147], v[66:69], v[144:147], v[126:129]
	v_exp_f32_e32 v148, v161
	v_fma_f32 v149, v156, v165, v149
	v_exp_f32_e32 v149, v149
	v_mfma_f32_16x16x32_f16 v[182:185], v[6:9], v[152:155], v[182:185]
	v_add_f32_e32 v148, 1.0, v148
	v_rcp_f32_e32 v156, v148
	v_add_f32_e32 v148, 1.0, v149
	v_mfma_f32_16x16x32_f16 v[226:229], v[46:49], v[152:155], v[226:229]
	v_rcp_f32_e32 v157, v148
	v_cmp_eq_u32_e32 vcc, s20, v214
	v_add_u32_e32 v173, 0x1000, v225
	v_mfma_f32_16x16x32_f16 v[144:147], v[70:73], v[152:155], v[144:147]
	v_cndmask_b32_e64 v1, v1, 0, vcc
	v_mfma_f32_16x16x32_f16 v[152:155], v[50:53], v[168:171], v[182:185]
	v_mfma_f32_16x16x32_f16 v[182:185], v[18:21], v[168:171], v[226:229]
	v_mfma_f32_16x16x32_f16 v[144:147], v[74:77], v[168:171], v[144:147]
	ds_read_b128 v[168:171], v142 offset:0x1000
	s_waitcnt lgkmcnt(5)
	s_nop 0
	v_mfma_f32_16x16x32_f16 v[152:155], v[10:13], v[174:177], v[152:155]
	v_mfma_f32_16x16x32_f16 v[182:185], v[58:61], v[174:177], v[182:185]
	v_mfma_f32_16x16x32_f16 v[146:149], v[90:93], v[174:177], v[144:147]
	s_nop 3
	v_fma_f32 v144, v157, -2.0, 1.0
	v_fma_f32 v144, -v156, v144, v144
	v_fma_mixlo_f16 v144, v156, v234, v144 op_sel:[0,1,0] op_sel_hi:[0,1,0]
	v_cndmask_b32_e64 v144, v144, 0, vcc
	s_mov_b32 m0, s40
	ds_read_b128 v[174:177], v201 offset:0x2000
	s_waitcnt lgkmcnt(4)
	ds_read_b128 v[226:229], v202 offset:0x2000
	s_waitcnt lgkmcnt(4)
	v_exp_f32_e32 v145, v158
	global_load_lds_dwordx4 v240, s[12:13]
	v_exp_f32_e32 v156, v162
	v_add_f32_e32 v145, 1.0, v145
	v_rcp_f32_e32 v145, v145
	v_mfma_f32_16x16x32_f16 v[152:155], v[14:17], v[178:181], v[152:155]
	v_pack_b32_f16 v144, v1, v144
	v_fma_f32 v145, v145, v166, v150
	v_add_f32_e32 v150, 1.0, v156
	v_rcp_f32_e32 v234, v150
	v_exp_f32_e32 v150, v159
	v_mfma_f32_16x16x32_f16 v[182:185], v[22:25], v[178:181], v[182:185]
	v_exp_f32_e32 v145, v145
	v_add_f32_e32 v150, 1.0, v150
	v_mfma_f32_16x16x32_f16 v[178:181], v[86:89], v[178:181], v[130:133]
	v_rcp_f32_e32 v150, v150
	v_add_f32_e32 v145, 1.0, v145
	v_rcp_f32_e32 v145, v145
	v_mfma_f32_16x16x32_f16 v[182:185], v[34:37], v[186:189], v[182:185]
	v_fmac_f32_e32 v151, v150, v167
	v_fma_f32 v145, v145, -2.0, 1.0
	v_mfma_f32_16x16x32_f16 v[178:181], v[78:81], v[186:189], v[178:181]
	v_fma_f32 v145, -v234, v145, v145
	v_fma_mixlo_f16 v145, v234, v235, v145 op_sel_hi:[0,1,0]
	v_cndmask_b32_e64 v145, v145, 0, vcc
	v_mfma_f32_16x16x32_f16 v[152:155], v[26:29], v[186:189], v[152:155]
	ds_read_b128 v[186:189], v203 offset:0x2000
	s_waitcnt lgkmcnt(4)
	ds_read_b128 v[164:167], v204 offset:0x2000
	s_waitcnt lgkmcnt(4)
	s_nop 0
	v_mfma_f32_16x16x32_f16 v[156:159], v[38:41], v[230:233], v[182:185]
	s_nop 2
	v_exp_f32_e32 v182, v163
	v_mfma_f32_16x16x32_f16 v[160:163], v[82:85], v[230:233], v[178:181]
	s_nop 2
	v_exp_f32_e32 v178, v151
	v_mfma_f32_16x16x32_f16 v[152:155], v[30:33], v[230:233], v[152:155]
	v_add_f32_e32 v179, 1.0, v182
	v_add_f32_e32 v178, 1.0, v178
	v_mfma_f32_16x16x32_f16 v[150:153], v[54:57], v[168:171], v[152:155]
	v_mfma_f32_16x16x32_f16 v[154:157], v[62:65], v[168:171], v[156:159]
	s_nop 2
	v_rcp_f32_e32 v158, v178
	v_rcp_f32_e32 v159, v179
	v_mfma_f32_16x16x32_f16 v[168:171], v[94:97], v[168:171], v[160:163]
	v_fma_f32 v158, v158, -2.0, 1.0
	v_fma_f32 v158, -v159, v158, v158
	v_fma_mixlo_f16 v158, v159, v235, v158 op_sel:[0,1,0] op_sel_hi:[0,1,0]
	v_cndmask_b32_e64 v158, v158, 0, vcc
	v_pack_b32_f16 v145, v145, v158
	global_store_dwordx2 v173, v[144:145], s[0:1] nt
	s_mov_b32 m0, s36
	ds_read_b64 v[238:239], v0 offset:0x1000
	ds_read_b128 v[178:181], v172 offset:0x2000
	s_waitcnt lgkmcnt(5)
	ds_read_b128 v[182:185], v223 offset:0x2000
	s_waitcnt lgkmcnt(5)
	v_exp_f32_e32 v1, v150
	s_waitcnt lgkmcnt(2)
	ds_read_b128 v[234:237], v143 offset:0x2000
	s_waitcnt lgkmcnt(5)
	global_load_lds_dwordx4 v243, s[12:13]
	v_add_f32_e32 v1, 1.0, v1
	v_rcp_f32_e32 v1, v1
	v_exp_f32_e32 v145, v151
	v_mfma_f32_16x16x32_f16 v[158:161], v[2:5], v[174:177], v[118:121]
	v_exp_f32_e32 v144, v154
	v_fma_f32 v1, v1, v168, v146
	v_exp_f32_e32 v1, v1
	v_mfma_f32_16x16x32_f16 v[230:233], v[42:45], v[174:177], v[122:125]
	v_add_f32_e32 v145, 1.0, v145
	v_rcp_f32_e32 v145, v145
	v_add_f32_e32 v1, 1.0, v1
	v_mfma_f32_16x16x32_f16 v[174:177], v[66:69], v[174:177], v[126:129]
	v_add_f32_e32 v144, 1.0, v144
	v_rcp_f32_e32 v1, v1
	v_rcp_f32_e32 v144, v144
	v_mfma_f32_16x16x32_f16 v[158:161], v[6:9], v[226:229], v[158:161]
	v_fma_f32 v145, v145, v169, v147
	v_exp_f32_e32 v145, v145
	v_exp_f32_e32 v146, v155
	v_mfma_f32_16x16x32_f16 v[174:177], v[70:73], v[226:229], v[174:177]
	v_fma_f32 v1, v1, -2.0, 1.0
	v_fma_f32 v1, -v144, v1, v1
	v_fma_mixlo_f16 v240, v144, v238, v1 op_sel_hi:[0,1,0]
	v_mfma_f32_16x16x32_f16 v[230:233], v[46:49], v[226:229], v[230:233]
	v_add_f32_e32 v144, 1.0, v145
	v_add_f32_e32 v1, 1.0, v146
	v_rcp_f32_e32 v150, v144
	v_mfma_f32_16x16x32_f16 v[158:161], v[50:53], v[186:189], v[158:161]
	v_rcp_f32_e32 v1, v1
	v_add_u32_e32 v173, 0x2000, v225
	v_fma_f32 v150, v150, -2.0, 1.0
	v_mfma_f32_16x16x32_f16 v[174:177], v[74:77], v[186:189], v[174:177]
	v_fma_f32 v243, -v1, v150, v150
	v_mfma_f32_16x16x32_f16 v[226:229], v[18:21], v[186:189], v[230:233]
	ds_read_b128 v[186:189], v142 offset:0x2000
	s_waitcnt lgkmcnt(5)
	s_nop 0
	v_mfma_f32_16x16x32_f16 v[158:161], v[10:13], v[164:167], v[158:161]
	v_mfma_f32_16x16x32_f16 v[144:147], v[90:93], v[164:167], v[174:177]
	v_mfma_f32_16x16x32_f16 v[226:229], v[58:61], v[164:167], v[226:229]
	s_mov_b32 m0, s35
	ds_read_b128 v[230:233], v201 offset:0x3000
	s_waitcnt lgkmcnt(4)
	v_exp_f32_e32 v150, v152
	v_mfma_f32_16x16x32_f16 v[164:167], v[14:17], v[178:181], v[158:161]
	ds_read_b128 v[160:163], v202 offset:0x3000
	s_waitcnt lgkmcnt(4)
	global_load_lds_dwordx4 v242, s[12:13]
	v_exp_f32_e32 v154, v153
	v_add_f32_e32 v150, 1.0, v150
	v_rcp_f32_e32 v150, v150
	v_mfma_f32_16x16x32_f16 v[174:177], v[22:25], v[178:181], v[226:229]
	v_add_f32_e32 v154, 1.0, v154
	v_rcp_f32_e32 v154, v154
	v_exp_f32_e32 v151, v156
	v_mfma_f32_16x16x32_f16 v[178:181], v[86:89], v[178:181], v[130:133]
	v_fma_f32 v148, v150, v170, v148
	v_exp_f32_e32 v148, v148
	v_fmac_f32_e32 v149, v154, v171
	v_mfma_f32_16x16x32_f16 v[226:229], v[26:29], v[182:185], v[164:167]
	v_exp_f32_e32 v149, v149
	v_add_f32_e32 v150, 1.0, v151
	v_rcp_f32_e32 v241, v150
	v_mfma_f32_16x16x32_f16 v[174:177], v[34:37], v[182:185], v[174:177]
	v_add_f32_e32 v148, 1.0, v148
	ds_read_b128 v[164:167], v203 offset:0x3000
	s_waitcnt lgkmcnt(4)
	v_mfma_f32_16x16x32_f16 v[178:181], v[78:81], v[182:185], v[178:181]
	v_exp_f32_e32 v155, v157
	v_rcp_f32_e32 v148, v148
	v_add_f32_e32 v149, 1.0, v149
	v_mfma_f32_16x16x32_f16 v[150:153], v[30:33], v[234:237], v[226:229]
	v_rcp_f32_e32 v149, v149
	ds_read_b128 v[168:171], v204 offset:0x3000
	s_waitcnt lgkmcnt(4)
	v_mfma_f32_16x16x32_f16 v[174:177], v[38:41], v[234:237], v[174:177]
	v_fma_f32 v148, v148, -2.0, 1.0
	v_fma_f32 v148, -v241, v148, v148
	v_fma_mixlo_f16 v241, v241, v239, v148 op_sel_hi:[0,1,0]
	v_mfma_f32_16x16x32_f16 v[178:181], v[82:85], v[234:237], v[178:181]
	v_fma_mixhi_f16 v240, v1, v238, v243 op_sel:[0,1,0] op_sel_hi:[0,1,0]
	v_mfma_f32_16x16x32_f16 v[156:159], v[54:57], v[186:189], v[150:153]
	s_nop 2
	v_add_f32_e32 v150, 1.0, v155
	v_mfma_f32_16x16x32_f16 v[152:155], v[62:65], v[186:189], v[174:177]
	s_nop 2
	v_rcp_f32_e32 v174, v150
	v_fma_f32 v175, v149, -2.0, 1.0
	v_mfma_f32_16x16x32_f16 v[148:151], v[94:97], v[186:189], v[178:181]
	v_fma_f32 v175, -v174, v175, v175
	v_fma_mixhi_f16 v241, v174, v239, v175 op_sel:[0,1,0] op_sel_hi:[0,1,0]
	global_store_dwordx2 v173, v[240:241], s[0:1] nt
	ds_read_b64 v[188:189], v0 offset:0x2000
	ds_read_b64 v[0:1], v0 offset:0x3000
	ds_read_b128 v[172:175], v172 offset:0x3000
	s_waitcnt lgkmcnt(6)
	s_andn2_b64 vcc, exec, s[10:11]
	v_mfma_f32_16x16x32_f16 v[180:183], v[2:5], v[230:233], v[118:121]
	s_waitcnt vmcnt(14)
	v_mfma_f32_16x16x32_f16 v[176:179], v[42:45], v[230:233], v[122:125]
	v_mfma_f32_16x16x32_f16 v[184:187], v[66:69], v[230:233], v[126:129]
	s_cbranch_vccnz .LBB5_11
	v_cvt_f16_f32_e32 v226, v134
	v_cvt_f16_f32_e32 v227, v135
	v_cvt_f16_f32_e32 v228, v136
	v_cvt_f16_f32_e32 v229, v137
	v_cvt_f16_f32_e32 v230, v138
	v_cvt_f16_f32_e32 v231, v139
	v_cvt_f16_f32_e32 v232, v140
	v_cvt_f16_f32_e32 v233, v141
	v_cmp_gt_i32_e32 vcc, s8, v224
	s_nop 1
	v_cndmask_b32_e32 v224, 0, v226, vcc
	v_cndmask_b32_e32 v226, 0, v227, vcc
	v_cndmask_b32_e32 v227, 0, v228, vcc
	v_cndmask_b32_e32 v234, 0, v229, vcc
	v_cndmask_b32_e32 v228, 0, v230, vcc
	v_cndmask_b32_e32 v230, 0, v231, vcc
	v_cndmask_b32_e32 v229, 0, v232, vcc
	v_cndmask_b32_e32 v231, 0, v233, vcc
	v_pack_b32_f16 v229, v229, v231
	v_pack_b32_f16 v228, v228, v230
	v_pack_b32_f16 v227, v227, v234
	v_pack_b32_f16 v226, v224, v226
	ds_write_b128 v220, v[226:229]
	s_branch .LBB5_11
.LBB5_16:
	v_exp_f32_e32 v2, v146
	v_exp_f32_e32 v4, v147
	v_exp_f32_e32 v3, v150
	v_exp_f32_e32 v6, v151
	v_add_f32_e32 v2, 1.0, v2
	v_rcp_f32_e32 v2, v2
	v_add_f32_e32 v4, 1.0, v4
	v_rcp_f32_e32 v4, v4
	v_add_f32_e32 v3, 1.0, v3
	v_fma_f32 v2, v154, v2, v142
	v_exp_f32_e32 v5, v2
	v_fma_f32 v2, v155, v4, v143
	v_exp_f32_e32 v7, v2
	v_rcp_f32_e32 v2, v3
	v_add_f32_e32 v3, 1.0, v5
	v_rcp_f32_e32 v4, v3
	v_add_f32_e32 v3, 1.0, v7
	v_rcp_f32_e32 v5, v3
	v_add_f32_e32 v3, 1.0, v6
	v_rcp_f32_e32 v3, v3
	v_cvt_f32_f16_sdwa v7, v0 dst_sel:DWORD dst_unused:UNUSED_PAD src0_sel:WORD_1
	v_cvt_f32_f16_e32 v6, v0
	v_pk_fma_f32 v[4:5], v[4:5], 2.0, 1.0 op_sel_hi:[1,0,0] neg_lo:[1,0,0] neg_hi:[1,0,0]
	v_exp_f32_e32 v8, v148
	v_pk_fma_f32 v[4:5], v[2:3], v[4:5], v[4:5] neg_lo:[1,0,0] neg_hi:[1,0,0]
	v_cvt_f32_f16_sdwa v9, v1 dst_sel:DWORD dst_unused:UNUSED_PAD src0_sel:WORD_1
	v_pk_fma_f32 v[2:3], v[2:3], v[6:7], v[4:5]
	v_exp_f32_e32 v4, v149
	v_add_f32_e32 v0, 1.0, v8
	v_rcp_f32_e32 v0, v0
	v_exp_f32_e32 v8, v152
	v_add_f32_e32 v4, 1.0, v4
	v_rcp_f32_e32 v6, v4
	v_fma_f32 v0, v156, v0, v144
	v_add_f32_e32 v5, 1.0, v8
	v_exp_f32_e32 v0, v0
	v_rcp_f32_e32 v4, v5
	v_exp_f32_e32 v5, v153
	v_fmac_f32_e32 v145, v157, v6
	v_exp_f32_e32 v7, v145
	v_add_f32_e32 v0, 1.0, v0
	v_rcp_f32_e32 v6, v0
	v_add_f32_e32 v0, 1.0, v5
	v_rcp_f32_e32 v5, v0
	v_add_f32_e32 v0, 1.0, v7
	v_rcp_f32_e32 v7, v0
	v_cvt_f32_f16_e32 v8, v1
	v_cvt_pk_f16_f32 v0, v2, v3
	s_lshl_b32 s2, s28, 14
	v_pk_fma_f32 v[2:3], v[6:7], 2.0, 1.0 op_sel_hi:[1,0,0] neg_lo:[1,0,0] neg_hi:[1,0,0]
	v_or_b32_e32 v10, v195, v206
	v_pk_fma_f32 v[2:3], v[4:5], v[2:3], v[2:3] neg_lo:[1,0,0] neg_hi:[1,0,0]
	s_add_i32 s2, s2, s15
	v_pk_fma_f32 v[2:3], v[4:5], v[8:9], v[2:3]
	s_nop 0
	v_cvt_pk_f16_f32 v1, v2, v3
	v_add_u32_e32 v2, s2, v10
	v_add_u32_e32 v2, 0x3000, v2
	global_store_dwordx2 v2, v[0:1], s[0:1] nt
	s_waitcnt vmcnt(0)
	s_endpgm
	.p2alignl 8, 3212836864

.LBB6_13:
	s_or_b64 exec, exec, s[2:3]
	v_exp_f32_e32 v134, v154
	ds_read_b128 v[138:141], v207 offset:0x3000
	s_waitcnt lgkmcnt(6)
	v_exp_f32_e32 v146, v146
	v_add_f32_e32 v154, 1.0, v134
	v_rcp_f32_e32 v154, v154
	v_mfma_f32_16x16x32_f16 v[134:137], v[6:9], v[162:165], v[182:185]
	s_waitcnt lgkmcnt(3)
	v_add_f32_e32 v146, 1.0, v146
	v_fma_f32 v142, v154, v150, v142
	v_exp_f32_e32 v150, v155
	v_exp_f32_e32 v142, v142
	v_mfma_f32_16x16x32_f16 v[174:177], v[46:49], v[162:165], v[174:177]
	v_rcp_f32_e32 v146, v146
	v_add_f32_e32 v150, 1.0, v150
	v_rcp_f32_e32 v150, v150
	v_mfma_f32_16x16x32_f16 v[162:165], v[70:73], v[162:165], v[178:181]
	ds_read_b128 v[178:181], v208 offset:0x3000
	s_waitcnt lgkmcnt(6)
	v_add_f32_e32 v142, 1.0, v142
	v_mfma_f32_16x16x32_f16 v[134:137], v[50:53], v[166:169], v[134:137]
	v_rcp_f32_e32 v142, v142
	v_fma_f32 v143, v150, v151, v143
	v_exp_f32_e32 v147, v147
	v_mfma_f32_16x16x32_f16 v[174:177], v[18:21], v[166:169], v[174:177]
	v_fma_f32 v142, v142, -2.0, 1.0
	v_fma_f32 v142, -v146, v142, v142
	v_add_u32_e32 v220, 0x3000, v218
	v_mfma_f32_16x16x32_f16 v[162:165], v[74:77], v[166:169], v[162:165]
	ds_read_b128 v[166:169], v209 offset:0x3000
	s_waitcnt lgkmcnt(6)
	v_fma_mixlo_f16 v218, v146, v188, v142 op_sel_hi:[0,1,0]
	v_mfma_f32_16x16x32_f16 v[182:185], v[10:13], v[158:161], v[134:137]
	s_add_i32 s2, s22, s10
	s_nop 1
	v_exp_f32_e32 v134, v143
	v_add_f32_e32 v135, 1.0, v147
	v_rcp_f32_e32 v221, v135
	v_mfma_f32_16x16x32_f16 v[174:177], v[58:61], v[158:161], v[174:177]
	v_add_f32_e32 v134, 1.0, v134
	v_rcp_f32_e32 v142, v134
	v_mfma_f32_16x16x32_f16 v[134:137], v[90:93], v[158:161], v[162:165]
	v_fma_f32 v142, v142, -2.0, 1.0
	v_fma_f32 v222, -v221, v142, v142
	v_exp_f32_e32 v142, v156
	v_exp_f32_e32 v143, v148
	s_waitcnt lgkmcnt(3)
	s_waitcnt lgkmcnt(2)
	v_add_f32_e32 v142, 1.0, v142
	v_rcp_f32_e32 v142, v142
	v_add_f32_e32 v143, 1.0, v143
	v_mfma_f32_16x16x32_f16 v[162:165], v[22:25], v[170:173], v[174:177]
	s_waitcnt lgkmcnt(1)
	v_fma_f32 v142, v142, v152, v144
	v_exp_f32_e32 v142, v142
	v_mfma_f32_16x16x32_f16 v[158:161], v[14:17], v[170:173], v[182:185]
	v_rcp_f32_e32 v174, v143
	v_exp_f32_e32 v143, v157
	v_add_f32_e32 v142, 1.0, v142
	v_mfma_f32_16x16x32_f16 v[170:173], v[86:89], v[170:173], v[130:133]
	v_rcp_f32_e32 v142, v142
	v_add_f32_e32 v143, 1.0, v143
	v_rcp_f32_e32 v143, v143
	v_mfma_f32_16x16x32_f16 v[158:161], v[26:29], v[138:141], v[158:161]
	v_fma_f32 v142, v142, -2.0, 1.0
	s_waitcnt lgkmcnt(0)
	v_fmac_f32_e32 v145, v143, v153
	v_mfma_f32_16x16x32_f16 v[162:165], v[34:37], v[138:141], v[162:165]
	v_exp_f32_e32 v143, v145
	v_fma_mixhi_f16 v218, v221, v188, v222 op_sel:[0,1,0] op_sel_hi:[0,1,0]
	v_mfma_f32_16x16x32_f16 v[138:141], v[78:81], v[138:141], v[170:173]
	v_mfma_f32_16x16x32_f16 v[154:157], v[30:33], v[178:181], v[158:161]
	s_nop 2
	v_fma_f32 v158, -v174, v142, v142
	v_exp_f32_e32 v142, v149
	v_mfma_f32_16x16x32_f16 v[150:153], v[82:85], v[178:181], v[138:141]
	v_fma_mixlo_f16 v219, v174, v189, v158 op_sel_hi:[0,1,0]
	v_add_f32_e32 v159, 1.0, v142
	s_nop 0
	v_add_f32_e32 v138, 1.0, v143
	v_rcp_f32_e32 v138, v138
	v_mfma_f32_16x16x32_f16 v[146:149], v[38:41], v[178:181], v[162:165]
	v_mfma_f32_16x16x32_f16 v[142:145], v[54:57], v[166:169], v[154:157]
	s_nop 2
	v_rcp_f32_e32 v154, v159
	v_fma_f32 v155, v138, -2.0, 1.0
	v_mfma_f32_16x16x32_f16 v[138:141], v[62:65], v[166:169], v[146:149]
	s_nop 2
	v_fma_f32 v146, -v154, v155, v155
	v_fma_mixhi_f16 v219, v154, v189, v146 op_sel:[0,1,0] op_sel_hi:[0,1,0]
	v_mfma_f32_16x16x32_f16 v[146:149], v[94:97], v[166:169], v[150:153]
	global_store_dwordx2 v220, v[218:219], s[0:1] nt
	s_add_i32 s16, s16, s21
	s_addk_i32 s19, 0x1000
	v_add_u32_e32 v210, s20, v210
	s_cmp_lt_i32 s2, s17
	v_add_u32_e32 v214, s20, v214
	s_waitcnt lgkmcnt(0)
	s_cbranch_scc0 .LBB6_18
.LBB6_14:
	s_and_b32 s23, s19, 0x1000
	v_or_b32_e32 v150, s23, v202
	v_cndmask_b32_e64 v150, v217, v150, s[4:5]
	s_waitcnt lgkmcnt(0)
	s_barrier
	v_add_u32_e32 v166, 0, v150
	ds_read_b128 v[150:153], v166
	ds_read_b128 v[154:157], v166 offset:1024
	ds_read_b128 v[158:161], v166 offset:3072
	ds_read_b128 v[162:165], v166 offset:2048
	s_waitcnt lgkmcnt(0)
	v_mfma_f32_16x16x32_f16 v[150:153], v[102:105], v[150:153], 0
	v_add_u32_e32 v167, 0, v203
	v_add_u32_e32 v168, 0x18000, v167
	s_mov_b32 s22, s2
	v_mfma_f32_16x16x32_f16 v[154:157], v[102:105], v[154:157], 0
	s_nop 3
	v_max_i32_e32 v151, 0, v151
	v_max_i32_e32 v150, 0, v150
	v_max_i32_e32 v153, 0, v153
	v_mfma_f32_16x16x32_f16 v[162:165], v[102:105], v[162:165], 0
	v_max_i32_e32 v152, 0, v152
	v_max_i32_e32 v155, 0, v155
	v_max_i32_e32 v154, 0, v154
	v_mfma_f32_16x16x32_f16 v[158:161], v[102:105], v[158:161], 0
	v_add_f32_e64 v150, v150, v154
	v_add_f32_e64 v151, v151, v155
	s_nop 1
	v_max_i32_e32 v155, 0, v163
	v_max_i32_e32 v154, 0, v162
	v_pk_add_f32 v[150:151], v[150:151], v[154:155]
	v_max_i32_e32 v155, 0, v157
	v_max_i32_e32 v154, 0, v156
	v_pk_add_f32 v[152:153], v[152:153], v[154:155]
	v_max_i32_e32 v155, 0, v165
	v_max_i32_e32 v154, 0, v164
	v_max_i32_e32 v158, 0, v158
	v_max_i32_e32 v159, 0, v159
	v_max_i32_e32 v160, 0, v160
	v_max_i32_e32 v161, 0, v161
	v_pk_add_f32 v[152:153], v[152:153], v[154:155]
	v_cvt_pk_f16_f32 v150, v150, v151
	v_cvt_pk_f16_f32 v151, v152, v153
	v_cvt_pk_f16_f32 v153, v160, v161
	v_cvt_pk_f16_f32 v152, v158, v159
	ds_write_b64 v167, v[150:151]
	ds_write_b64 v168, v[152:153]
	ds_read_b128 v[150:153], v166 offset:256
	ds_read_b128 v[154:157], v166 offset:1280
	ds_read_b128 v[158:161], v166 offset:2304
	ds_read_b128 v[162:165], v166 offset:3328
	s_waitcnt lgkmcnt(3)
	v_mfma_f32_16x16x32_f16 v[150:153], v[102:105], v[150:153], 0
	v_subrev_co_u32_e32 v215, vcc, 1, v215
	s_waitcnt lgkmcnt(2)
	v_mfma_f32_16x16x32_f16 v[154:157], v[102:105], v[154:157], 0
	s_nop 4
	v_max_i32_e32 v151, 0, v151
	v_max_i32_e32 v150, 0, v150
	v_max_i32_e32 v153, 0, v153
	s_waitcnt lgkmcnt(1)
	v_mfma_f32_16x16x32_f16 v[158:161], v[102:105], v[158:161], 0
	v_max_i32_e32 v152, 0, v152
	v_max_i32_e32 v155, 0, v155
	v_max_i32_e32 v154, 0, v154
	s_waitcnt lgkmcnt(0)
	v_mfma_f32_16x16x32_f16 v[162:165], v[102:105], v[162:165], 0
	v_add_f32_e64 v150, v150, v154
	v_add_f32_e64 v151, v151, v155
	s_nop 0
	v_max_i32_e32 v155, 0, v159
	v_max_i32_e32 v154, 0, v158
	v_pk_add_f32 v[150:151], v[150:151], v[154:155]
	v_max_i32_e32 v155, 0, v157
	v_max_i32_e32 v154, 0, v156
	v_pk_add_f32 v[152:153], v[152:153], v[154:155]
	v_max_i32_e32 v155, 0, v161
	v_max_i32_e32 v154, 0, v160
	v_pk_add_f32 v[152:153], v[152:153], v[154:155]
	v_max_i32_e32 v162, 0, v162
	v_max_i32_e32 v163, 0, v163
	v_max_i32_e32 v164, 0, v164
	v_max_i32_e32 v165, 0, v165
	v_cvt_pk_f16_f32 v150, v150, v151
	v_cvt_pk_f16_f32 v151, v152, v153
	v_cvt_pk_f16_f32 v153, v164, v165
	v_cvt_pk_f16_f32 v152, v162, v163
	ds_write_b64 v167, v[150:151] offset:4096
	ds_write_b64 v168, v[152:153] offset:4096
	ds_read_b128 v[150:153], v166 offset:512
	ds_read_b128 v[154:157], v166 offset:1536
	ds_read_b128 v[158:161], v166 offset:2560
	ds_read_b128 v[162:165], v166 offset:3584
	s_waitcnt lgkmcnt(3)
	v_mfma_f32_16x16x32_f16 v[150:153], v[102:105], v[150:153], 0
	s_waitcnt lgkmcnt(2)
	v_mfma_f32_16x16x32_f16 v[154:157], v[102:105], v[154:157], 0
	s_nop 5
	v_max_i32_e32 v151, 0, v151
	v_max_i32_e32 v150, 0, v150
	v_max_i32_e32 v153, 0, v153
	s_waitcnt lgkmcnt(1)
	v_mfma_f32_16x16x32_f16 v[158:161], v[102:105], v[158:161], 0
	v_max_i32_e32 v152, 0, v152
	v_max_i32_e32 v155, 0, v155
	v_max_i32_e32 v154, 0, v154
	s_waitcnt lgkmcnt(0)
	v_mfma_f32_16x16x32_f16 v[162:165], v[102:105], v[162:165], 0
	v_add_f32_e64 v150, v150, v154
	v_add_f32_e64 v151, v151, v155
	s_nop 0
	v_max_i32_e32 v155, 0, v159
	v_max_i32_e32 v154, 0, v158
	v_pk_add_f32 v[150:151], v[150:151], v[154:155]
	v_max_i32_e32 v155, 0, v157
	v_max_i32_e32 v154, 0, v156
	v_pk_add_f32 v[152:153], v[152:153], v[154:155]
	v_max_i32_e32 v155, 0, v161
	v_max_i32_e32 v154, 0, v160
	v_pk_add_f32 v[152:153], v[152:153], v[154:155]
	v_max_i32_e32 v162, 0, v162
	v_max_i32_e32 v163, 0, v163
	v_max_i32_e32 v164, 0, v164
	v_max_i32_e32 v165, 0, v165
	v_cvt_pk_f16_f32 v150, v150, v151
	v_cvt_pk_f16_f32 v151, v152, v153
	v_cvt_pk_f16_f32 v153, v164, v165
	v_cvt_pk_f16_f32 v152, v162, v163
	ds_write_b64 v167, v[150:151] offset:8192
	ds_write_b64 v168, v[152:153] offset:8192
	ds_read_b128 v[150:153], v166 offset:768
	ds_read_b128 v[154:157], v166 offset:1792
	ds_read_b128 v[158:161], v166 offset:2816
	ds_read_b128 v[162:165], v166 offset:3840
	s_waitcnt lgkmcnt(3)
	v_mfma_f32_16x16x32_f16 v[150:153], v[102:105], v[150:153], 0
	s_waitcnt lgkmcnt(2)
	v_mfma_f32_16x16x32_f16 v[154:157], v[102:105], v[154:157], 0
	s_nop 5
	v_max_i32_e32 v151, 0, v151
	v_max_i32_e32 v150, 0, v150
	v_max_i32_e32 v153, 0, v153
	s_waitcnt lgkmcnt(1)
	v_mfma_f32_16x16x32_f16 v[158:161], v[102:105], v[158:161], 0
	v_max_i32_e32 v152, 0, v152
	v_max_i32_e32 v155, 0, v155
	v_max_i32_e32 v154, 0, v154
	s_waitcnt lgkmcnt(0)
	v_mfma_f32_16x16x32_f16 v[162:165], v[102:105], v[162:165], 0
	v_add_f32_e64 v150, v150, v154
	v_add_f32_e64 v151, v151, v155
	s_nop 0
	v_max_i32_e32 v155, 0, v159
	v_max_i32_e32 v154, 0, v158
	v_pk_add_f32 v[150:151], v[150:151], v[154:155]
	v_max_i32_e32 v155, 0, v157
	v_max_i32_e32 v154, 0, v156
	v_pk_add_f32 v[152:153], v[152:153], v[154:155]
	v_max_i32_e32 v155, 0, v161
	v_max_i32_e32 v154, 0, v160
	v_pk_add_f32 v[152:153], v[152:153], v[154:155]
	v_max_i32_e32 v162, 0, v162
	v_max_i32_e32 v163, 0, v163
	v_max_i32_e32 v164, 0, v164
	v_max_i32_e32 v165, 0, v165
	v_cvt_pk_f16_f32 v150, v150, v151
	v_cvt_pk_f16_f32 v151, v152, v153
	v_cvt_pk_f16_f32 v153, v164, v165
	v_cvt_pk_f16_f32 v152, v162, v163
	ds_write_b64 v167, v[150:151] offset:12288
	ds_write_b64 v168, v[152:153] offset:12288
	s_waitcnt lgkmcnt(0)
	s_barrier
	ds_read_b128 v[150:153], v192 offset:0
	ds_read_b128 v[154:157], v192 offset:0x1000
	ds_read_b128 v[158:161], v192 offset:0x2000
	ds_read_b128 v[162:165], v192 offset:0x3000
	ds_read_b128 v[166:169], v194 offset:0
	s_nop 0
	s_waitcnt lgkmcnt(4)
	s_nop 0
	v_mfma_f32_16x16x32_f16 v[170:173], v[98:101], v[150:153], 0
	ds_read_b128 v[174:177], v194 offset:0x1000
	s_waitcnt lgkmcnt(4)
	s_nop 0
	v_mfma_f32_16x16x32_f16 v[178:181], v[98:101], v[154:157], 0
	ds_read_b128 v[182:185], v194 offset:0x2000
	s_waitcnt lgkmcnt(4)
	s_nop 0
	v_mfma_f32_16x16x32_f16 v[218:221], v[98:101], v[158:161], 0
	ds_read_b128 v[222:225], v194 offset:0x3000
	s_waitcnt lgkmcnt(4)
	s_nop 0
	v_mfma_f32_16x16x32_f16 v[226:229], v[98:101], v[162:165], 0
	ds_read_b128 v[150:153], v195 offset:0
	s_waitcnt lgkmcnt(4)
	s_nop 0
	v_mfma_f32_16x16x32_f16 v[166:169], v[110:113], v[166:169], v[170:173]
	ds_read_b128 v[154:157], v195 offset:0x1000
	s_waitcnt lgkmcnt(4)
	s_nop 0
	v_mfma_f32_16x16x32_f16 v[170:173], v[110:113], v[174:177], v[178:181]
	ds_read_b128 v[158:161], v195 offset:0x2000
	s_waitcnt lgkmcnt(4)
	s_nop 0
	v_mfma_f32_16x16x32_f16 v[174:177], v[110:113], v[182:185], v[218:221]
	ds_read_b128 v[162:165], v195 offset:0x3000
	s_waitcnt lgkmcnt(4)
	s_and_b64 vcc, exec, vcc
	v_mfma_f32_16x16x32_f16 v[178:181], v[110:113], v[222:225], v[226:229]
	s_cbranch_vccnz .LBB6_16
	v_exp_f32_e32 v142, v142
	v_exp_f32_e32 v143, v143
	v_exp_f32_e32 v138, v138
	v_exp_f32_e32 v139, v139
	v_add_f32_e32 v142, 1.0, v142
	v_rcp_f32_e32 v142, v142
	v_add_f32_e32 v143, 1.0, v143
	v_rcp_f32_e32 v143, v143
	v_add_f32_e32 v138, 1.0, v138
	v_fmac_f32_e32 v134, v146, v142
	v_exp_f32_e32 v142, v134
	v_fmac_f32_e32 v135, v147, v143
	v_exp_f32_e32 v143, v135
	v_rcp_f32_e32 v134, v138
	v_add_f32_e32 v135, 1.0, v142
	v_rcp_f32_e32 v138, v135
	v_add_f32_e32 v135, 1.0, v139
	v_add_f32_e32 v139, 1.0, v143
	v_rcp_f32_e32 v139, v139
	v_cvt_f32_f16_sdwa v143, v0 dst_sel:DWORD dst_unused:UNUSED_PAD src0_sel:WORD_1
	v_cvt_f32_f16_e32 v142, v0
	v_exp_f32_e32 v0, v144
	v_rcp_f32_e32 v135, v135
	v_pk_fma_f32 v[138:139], v[138:139], 2.0, 1.0 op_sel_hi:[1,0,0] neg_lo:[1,0,0] neg_hi:[1,0,0]
	v_exp_f32_e32 v140, v140
	v_add_f32_e32 v0, 1.0, v0
	v_pk_fma_f32 v[138:139], v[134:135], v[138:139], v[138:139] neg_lo:[1,0,0] neg_hi:[1,0,0]
	v_rcp_f32_e32 v0, v0
	v_pk_fma_f32 v[134:135], v[134:135], v[142:143], v[138:139]
	v_exp_f32_e32 v138, v145
	v_add_f32_e32 v139, 1.0, v140
	v_fmac_f32_e32 v136, v148, v0
	v_exp_f32_e32 v0, v136
	v_add_f32_e32 v136, 1.0, v138
	v_rcp_f32_e32 v138, v136
	v_rcp_f32_e32 v136, v139
	v_exp_f32_e32 v139, v141
	v_add_f32_e32 v0, 1.0, v0
	v_fmac_f32_e32 v137, v149, v138
	v_exp_f32_e32 v140, v137
	v_rcp_f32_e32 v138, v0
	v_add_f32_e32 v0, 1.0, v139
	v_rcp_f32_e32 v137, v0
	v_add_f32_e32 v0, 1.0, v140
	v_rcp_f32_e32 v139, v0
	v_cvt_f32_f16_sdwa v141, v1 dst_sel:DWORD dst_unused:UNUSED_PAD src0_sel:WORD_1
	v_cvt_f32_f16_e32 v140, v1
	v_cvt_pk_f16_f32 v0, v134, v135
	v_pk_fma_f32 v[134:135], v[138:139], 2.0, 1.0 op_sel_hi:[1,0,0] neg_lo:[1,0,0] neg_hi:[1,0,0]
	s_nop 0
	v_pk_fma_f32 v[134:135], v[136:137], v[134:135], v[134:135] neg_lo:[1,0,0] neg_hi:[1,0,0]
	s_nop 0
	v_pk_fma_f32 v[134:135], v[136:137], v[140:141], v[134:135]
	s_nop 0
	v_cvt_pk_f16_f32 v1, v134, v135
	v_add_u32_e32 v134, v193, v214
	global_store_dwordx2 v134, v[0:1], s[0:1] nt
.LBB6_16:
	v_or_b32_e32 v0, s23, v201
	v_cndmask_b32_e64 v0, v217, v0, s[4:5]
	ds_read_b128 v[134:137], v196 offset:0
	s_waitcnt lgkmcnt(4)
	s_nop 0
	v_mfma_f32_16x16x32_f16 v[138:141], v[114:117], v[150:153], v[166:169]
	ds_read_b128 v[142:145], v196 offset:0x1000
	s_waitcnt lgkmcnt(4)
	s_nop 0
	v_mfma_f32_16x16x32_f16 v[146:149], v[114:117], v[154:157], v[170:173]
	ds_read_b128 v[150:153], v196 offset:0x2000
	s_waitcnt lgkmcnt(4)
	s_nop 0
	v_mfma_f32_16x16x32_f16 v[154:157], v[114:117], v[158:161], v[174:177]
	ds_read_b128 v[158:161], v196 offset:0x3000
	s_waitcnt lgkmcnt(4)
	s_nop 0
	v_mfma_f32_16x16x32_f16 v[162:165], v[114:117], v[162:165], v[178:181]
	ds_read_b128 v[166:169], v0 offset:0
	s_waitcnt lgkmcnt(4)
	s_nop 0
	v_mfma_f32_16x16x32_f16 v[134:137], v[106:109], v[134:137], v[138:141]
	ds_read_b128 v[138:141], v0 offset:0x100
	s_waitcnt lgkmcnt(4)
	s_nop 0
	v_mfma_f32_16x16x32_f16 v[142:145], v[106:109], v[142:145], v[146:149]
	ds_read_b128 v[146:149], v0 offset:0x200
	s_waitcnt lgkmcnt(4)
	s_nop 0
	v_mfma_f32_16x16x32_f16 v[150:153], v[106:109], v[150:153], v[154:157]
	ds_read_b128 v[154:157], v0 offset:0x300
	s_waitcnt lgkmcnt(4)
	s_nop 0
	v_mfma_f32_16x16x32_f16 v[158:161], v[106:109], v[158:161], v[162:165]
	s_waitcnt lgkmcnt(3)
	s_nop 0
	v_mfma_f32_16x16x32_f16 v[134:137], v[102:105], v[166:169], v[134:137]
	s_waitcnt lgkmcnt(2)
	s_nop 0
	v_mfma_f32_16x16x32_f16 v[138:141], v[102:105], v[138:141], v[142:145]
	s_waitcnt lgkmcnt(1)
	s_nop 0
	v_mfma_f32_16x16x32_f16 v[142:145], v[102:105], v[146:149], v[150:153]
	s_waitcnt lgkmcnt(0)
	s_nop 0
	v_mfma_f32_16x16x32_f16 v[146:149], v[102:105], v[154:157], v[158:161]
	s_nop 1
	v_max_i32_e32 v0, 0, v134
	v_max_i32_e32 v134, 0, v135
	v_max_i32_e32 v1, 0, v136
	v_max_i32_e32 v135, 0, v137
	v_cvt_pk_f16_f32 v1, v1, v135
	v_cvt_pk_f16_f32 v0, v0, v134
	v_max_i32_e32 v134, 0, v138
	v_max_i32_e32 v136, 0, v139
	v_max_i32_e32 v135, 0, v140
	v_max_i32_e32 v137, 0, v141
	v_cvt_pk_f16_f32 v135, v135, v137
	v_cvt_pk_f16_f32 v134, v134, v136
	ds_write2st64_b64 v216, v[0:1], v[134:135] offset1:8
	v_max_i32_e32 v0, 0, v142
	v_max_i32_e32 v134, 0, v143
	v_max_i32_e32 v1, 0, v144
	v_max_i32_e32 v135, 0, v145
	v_cvt_pk_f16_f32 v1, v1, v135
	v_cvt_pk_f16_f32 v0, v0, v134
	v_max_i32_e32 v134, 0, v146
	v_max_i32_e32 v136, 0, v147
	v_max_i32_e32 v135, 0, v148
	v_max_i32_e32 v137, 0, v149
	v_cvt_pk_f16_f32 v135, v135, v137
	v_cvt_pk_f16_f32 v134, v134, v136
	ds_write2st64_b64 v216, v[0:1], v[134:135] offset0:16 offset1:24
	s_waitcnt lgkmcnt(0)
	s_barrier
	ds_read_b128 v[134:137], v197 offset:0
	ds_read_b128 v[138:141], v198 offset:0
	ds_read_b128 v[142:145], v199 offset:0
	ds_read_b128 v[146:149], v200 offset:0
	ds_read_b128 v[150:153], v206 offset:0
	v_add_u32_e32 v0, s16, v213
	s_waitcnt lgkmcnt(4)
	v_min_i32_e32 v0, s11, v0
	v_mfma_f32_16x16x32_f16 v[154:157], v[2:5], v[134:137], v[118:121]
	v_cndmask_b32_e64 v0, v190, v0, s[8:9]
	v_ashrrev_i32_e32 v1, 31, v0
	ds_read_b128 v[162:165], v207 offset:0
	v_mfma_f32_16x16x32_f16 v[158:161], v[42:45], v[134:137], v[122:125]
	s_waitcnt lgkmcnt(4)
	v_lshlrev_b64 v[0:1], 5, v[0:1]
	v_lshl_add_u64 v[0:1], s[14:15], 0, v[0:1]
	v_mfma_f32_16x16x32_f16 v[134:137], v[66:69], v[134:137], v[126:129]
	v_lshl_add_u64 v[170:171], v[0:1], 0, 16
	v_mfma_f32_16x16x32_f16 v[154:157], v[6:9], v[138:141], v[154:157]
	v_mfma_f32_16x16x32_f16 v[158:161], v[46:49], v[138:141], v[158:161]
	v_mfma_f32_16x16x32_f16 v[166:169], v[70:73], v[138:141], v[134:137]
	global_load_dwordx4 v[138:141], v[0:1], off
	global_load_dwordx4 v[134:137], v[170:171], off
	ds_read_b128 v[170:173], v208 offset:0
	s_waitcnt lgkmcnt(4)
	v_add_u32_e32 v0, s16, v212
	v_mfma_f32_16x16x32_f16 v[154:157], v[50:53], v[142:145], v[154:157]
	v_min_i32_e32 v0, s11, v0
	v_mad_i64_i32 v[0:1], s[2:3], v0, 12, s[12:13]
	v_mfma_f32_16x16x32_f16 v[158:161], v[18:21], v[142:145], v[158:161]
	v_lshl_add_u64 v[0:1], v[0:1], 0, v[186:187]
	global_load_dword v190, v[0:1], off
	v_mfma_f32_16x16x32_f16 v[142:145], v[74:77], v[142:145], v[166:169]
	ds_read_b128 v[166:169], v209 offset:0
	s_waitcnt lgkmcnt(4)
	s_nop 0
	v_mfma_f32_16x16x32_f16 v[154:157], v[10:13], v[146:149], v[154:157]
	v_mfma_f32_16x16x32_f16 v[158:161], v[58:61], v[146:149], v[158:161]
	v_mfma_f32_16x16x32_f16 v[146:149], v[90:93], v[146:149], v[142:145]
	ds_read_b128 v[142:145], v197 offset:0x1000
	s_waitcnt lgkmcnt(4)
	ds_read_b128 v[174:177], v198 offset:0x1000
	s_waitcnt lgkmcnt(4)
	s_nop 0
	v_mfma_f32_16x16x32_f16 v[154:157], v[14:17], v[150:153], v[154:157]
	v_mfma_f32_16x16x32_f16 v[158:161], v[22:25], v[150:153], v[158:161]
	v_mfma_f32_16x16x32_f16 v[150:153], v[86:89], v[150:153], v[130:133]
	v_mfma_f32_16x16x32_f16 v[154:157], v[26:29], v[162:165], v[154:157]
	v_mfma_f32_16x16x32_f16 v[158:161], v[34:37], v[162:165], v[158:161]
	v_mfma_f32_16x16x32_f16 v[150:153], v[78:81], v[162:165], v[150:153]
	ds_read_b128 v[162:165], v199 offset:0x1000
	s_waitcnt lgkmcnt(4)
	s_nop 0
	v_mfma_f32_16x16x32_f16 v[154:157], v[30:33], v[170:173], v[154:157]
	v_mfma_f32_16x16x32_f16 v[158:161], v[38:41], v[170:173], v[158:161]
	v_mfma_f32_16x16x32_f16 v[150:153], v[82:85], v[170:173], v[150:153]
	ds_read_b128 v[170:173], v200 offset:0x1000
	s_waitcnt lgkmcnt(4)
	s_nop 0
	v_mfma_f32_16x16x32_f16 v[154:157], v[54:57], v[166:169], v[154:157]
	v_mfma_f32_16x16x32_f16 v[158:161], v[62:65], v[166:169], v[158:161]
	v_mfma_f32_16x16x32_f16 v[150:153], v[94:97], v[166:169], v[150:153]
	s_nop 5
	v_exp_f32_e32 v154, v154
	v_exp_f32_e32 v158, v158
	ds_read_b64 v[0:1], v204 offset:0
	ds_read_b128 v[166:169], v206 offset:0x1000
	v_add_f32_e32 v154, 1.0, v154
	v_rcp_f32_e32 v154, v154
	v_add_f32_e32 v158, 1.0, v158
	s_waitcnt lgkmcnt(5)
	ds_read_b128 v[220:223], v207 offset:0x1000
	v_fma_f32 v146, v154, v150, v146
	v_exp_f32_e32 v146, v146
	v_exp_f32_e32 v154, v155
	v_rcp_f32_e32 v150, v158
	v_mfma_f32_16x16x32_f16 v[178:181], v[2:5], v[142:145], v[118:121]
	v_add_f32_e32 v146, 1.0, v146
	v_add_f32_e32 v154, 1.0, v154
	v_rcp_f32_e32 v146, v146
	v_rcp_f32_e32 v154, v154
	v_mfma_f32_16x16x32_f16 v[182:185], v[42:45], v[142:145], v[122:125]
	s_waitcnt lgkmcnt(5)
	v_fma_f32 v146, v146, -2.0, 1.0
	v_fma_f32 v147, v154, v151, v147
	v_mfma_f32_16x16x32_f16 v[142:145], v[66:69], v[142:145], v[126:129]
	v_fma_f32 v146, -v150, v146, v146
	v_exp_f32_e32 v147, v147
	s_waitcnt lgkmcnt(2)
	v_mfma_f32_16x16x32_f16 v[178:181], v[6:9], v[174:177], v[178:181]
	v_fma_mixlo_f16 v146, v150, v0, v146 op_sel_hi:[0,1,0]
	v_exp_f32_e32 v150, v159
	v_add_f32_e32 v147, 1.0, v147
	v_mfma_f32_16x16x32_f16 v[182:185], v[46:49], v[174:177], v[182:185]
	v_rcp_f32_e32 v151, v147
	v_add_f32_e32 v150, 1.0, v150
	v_rcp_f32_e32 v150, v150
	v_mfma_f32_16x16x32_f16 v[142:145], v[70:73], v[174:177], v[142:145]
	ds_read_b128 v[174:177], v208 offset:0x1000
	s_waitcnt lgkmcnt(5)
	v_cmp_eq_u32_e32 vcc, s16, v211
	v_mfma_f32_16x16x32_f16 v[178:181], v[50:53], v[162:165], v[178:181]
	v_add_u32_e32 v218, v193, v210
	v_cndmask_b32_e64 v189, v146, 0, vcc
	v_add_u32_e32 v188, 0x1000, v218
	v_mfma_f32_16x16x32_f16 v[182:185], v[18:21], v[162:165], v[182:185]
	v_mfma_f32_16x16x32_f16 v[142:145], v[74:77], v[162:165], v[142:145]
	ds_read_b128 v[162:165], v209 offset:0x1000
	s_waitcnt lgkmcnt(5)
	s_nop 0
	v_mfma_f32_16x16x32_f16 v[178:181], v[10:13], v[170:173], v[178:181]
	v_mfma_f32_16x16x32_f16 v[182:185], v[58:61], v[170:173], v[182:185]
	v_mfma_f32_16x16x32_f16 v[144:147], v[90:93], v[170:173], v[142:145]
	s_nop 3
	v_fma_f32 v142, v151, -2.0, 1.0
	v_fma_f32 v142, -v150, v142, v142
	v_fma_mixlo_f16 v0, v150, v0, v142 op_sel:[0,1,0] op_sel_hi:[0,1,0]
	v_cndmask_b32_e64 v0, v0, 0, vcc
	v_exp_f32_e32 v142, v156
	ds_read_b128 v[170:173], v197 offset:0x2000
	s_waitcnt lgkmcnt(4)
	v_exp_f32_e32 v143, v160
	v_add_f32_e32 v142, 1.0, v142
	v_rcp_f32_e32 v142, v142
	v_mfma_f32_16x16x32_f16 v[182:185], v[22:25], v[166:169], v[182:185]
	ds_read_b128 v[224:227], v198 offset:0x2000
	s_waitcnt lgkmcnt(4)
	v_fma_f32 v142, v142, v152, v148
	v_exp_f32_e32 v148, v157
	v_mfma_f32_16x16x32_f16 v[178:181], v[14:17], v[166:169], v[178:181]
	v_exp_f32_e32 v142, v142
	v_add_f32_e32 v143, 1.0, v143
	v_add_f32_e32 v148, 1.0, v148
	v_rcp_f32_e32 v148, v148
	v_mfma_f32_16x16x32_f16 v[166:169], v[86:89], v[166:169], v[130:133]
	v_add_f32_e32 v142, 1.0, v142
	v_rcp_f32_e32 v142, v142
	v_rcp_f32_e32 v143, v143
	v_mfma_f32_16x16x32_f16 v[182:185], v[34:37], v[220:223], v[182:185]
	v_fmac_f32_e32 v149, v148, v153
	v_exp_f32_e32 v150, v161
	v_fma_f32 v142, v142, -2.0, 1.0
	v_mfma_f32_16x16x32_f16 v[178:181], v[26:29], v[220:223], v[178:181]
	v_fma_f32 v142, -v143, v142, v142
	v_fma_mixlo_f16 v142, v143, v1, v142 op_sel_hi:[0,1,0]
	v_add_f32_e32 v143, 1.0, v150
	v_mfma_f32_16x16x32_f16 v[154:157], v[78:81], v[220:223], v[166:169]
	ds_read_b128 v[166:169], v199 offset:0x2000
	s_waitcnt lgkmcnt(4)
	v_rcp_f32_e32 v143, v143
	v_mfma_f32_16x16x32_f16 v[158:161], v[38:41], v[174:177], v[182:185]
	v_cndmask_b32_e64 v142, v142, 0, vcc
	v_pack_b32_f16 v0, v189, v0
	s_nop 0
	v_exp_f32_e32 v182, v149
	v_mfma_f32_16x16x32_f16 v[178:181], v[30:33], v[174:177], v[178:181]
	v_mfma_f32_16x16x32_f16 v[148:151], v[82:85], v[174:177], v[154:157]
	ds_read_b128 v[152:155], v200 offset:0x2000
	s_waitcnt lgkmcnt(4)
	s_nop 0
	v_mfma_f32_16x16x32_f16 v[174:177], v[54:57], v[162:165], v[178:181]
	s_nop 0
	v_add_f32_e32 v156, 1.0, v182
	s_nop 2
	v_rcp_f32_e32 v178, v156
	v_mfma_f32_16x16x32_f16 v[156:159], v[62:65], v[162:165], v[158:161]
	s_nop 2
	v_fma_f32 v160, v178, -2.0, 1.0
	v_fma_f32 v160, -v143, v160, v160
	v_mfma_f32_16x16x32_f16 v[148:151], v[94:97], v[162:165], v[148:151]
	v_fma_mixlo_f16 v1, v143, v1, v160 op_sel:[0,1,0] op_sel_hi:[0,1,0]
	v_cndmask_b32_e64 v1, v1, 0, vcc
	v_pack_b32_f16 v1, v142, v1
	global_store_dwordx2 v188, v[0:1], s[0:1] nt
	v_exp_f32_e32 v142, v174
	v_exp_f32_e32 v143, v156
	ds_read_b64 v[0:1], v204 offset:0x1000
	ds_read_b128 v[160:163], v206 offset:0x2000
	v_add_f32_e32 v142, 1.0, v142
	v_rcp_f32_e32 v142, v142
	s_waitcnt lgkmcnt(5)
	v_add_f32_e32 v143, 1.0, v143
	v_mfma_f32_16x16x32_f16 v[178:181], v[2:5], v[170:173], v[118:121]
	v_fma_f32 v142, v142, v148, v144
	v_exp_f32_e32 v144, v175
	v_exp_f32_e32 v142, v142
	v_mfma_f32_16x16x32_f16 v[182:185], v[42:45], v[170:173], v[122:125]
	v_rcp_f32_e32 v143, v143
	v_add_f32_e32 v144, 1.0, v144
	v_add_f32_e32 v142, 1.0, v142
	v_mfma_f32_16x16x32_f16 v[170:173], v[66:69], v[170:173], v[126:129]
	v_rcp_f32_e32 v144, v144
	v_rcp_f32_e32 v142, v142
	ds_read_b128 v[220:223], v207 offset:0x2000
	s_waitcnt lgkmcnt(5)
	v_fma_f32 v148, v144, v149, v145
	v_mfma_f32_16x16x32_f16 v[178:181], v[6:9], v[224:227], v[178:181]
	v_fma_f32 v142, v142, -2.0, 1.0
	v_exp_f32_e32 v148, v148
	v_fma_f32 v142, -v143, v142, v142
	v_mfma_f32_16x16x32_f16 v[182:185], v[46:49], v[224:227], v[182:185]
	v_exp_f32_e32 v149, v157
	s_waitcnt lgkmcnt(2)
	v_add_f32_e32 v148, 1.0, v148
	v_mfma_f32_16x16x32_f16 v[170:173], v[70:73], v[224:227], v[170:173]
	ds_read_b128 v[224:227], v208 offset:0x2000
	s_waitcnt lgkmcnt(5)
	v_fma_mixlo_f16 v188, v143, v0, v142 op_sel_hi:[0,1,0]
	v_mfma_f32_16x16x32_f16 v[178:181], v[50:53], v[166:169], v[178:181]
	v_rcp_f32_e32 v148, v148
	v_add_f32_e32 v149, 1.0, v149
	v_rcp_f32_e32 v232, v149
	v_mfma_f32_16x16x32_f16 v[182:185], v[18:21], v[166:169], v[182:185]
	v_fma_f32 v148, v148, -2.0, 1.0
	v_add_u32_e32 v219, 0x2000, v218
	v_fma_f32 v233, -v232, v148, v148
	v_mfma_f32_16x16x32_f16 v[142:145], v[74:77], v[166:169], v[170:173]
	ds_read_b128 v[170:173], v209 offset:0x2000
	s_waitcnt lgkmcnt(5)
	s_nop 0
	v_mfma_f32_16x16x32_f16 v[164:167], v[10:13], v[152:155], v[178:181]
	v_mfma_f32_16x16x32_f16 v[178:181], v[58:61], v[152:155], v[182:185]
	v_mfma_f32_16x16x32_f16 v[142:145], v[90:93], v[152:155], v[142:145]
	v_exp_f32_e32 v148, v176
	v_exp_f32_e32 v149, v158
	ds_read_b128 v[228:231], v197 offset:0x3000
	s_waitcnt lgkmcnt(4)
	v_add_f32_e32 v148, 1.0, v148
	v_rcp_f32_e32 v148, v148
	v_mfma_f32_16x16x32_f16 v[152:155], v[14:17], v[160:163], v[164:167]
	v_fma_mixhi_f16 v188, v232, v0, v233 op_sel:[0,1,0] op_sel_hi:[0,1,0]
	v_fma_f32 v146, v148, v150, v146
	v_add_f32_e32 v148, 1.0, v149
	v_exp_f32_e32 v149, v177
	v_mfma_f32_16x16x32_f16 v[166:169], v[22:25], v[160:163], v[178:181]
	v_exp_f32_e32 v146, v146
	v_exp_f32_e32 v150, v159
	v_add_f32_e32 v149, 1.0, v149
	v_rcp_f32_e32 v149, v149
	v_mfma_f32_16x16x32_f16 v[178:181], v[86:89], v[160:163], v[130:133]
	ds_read_b128 v[162:165], v198 offset:0x3000
	s_waitcnt lgkmcnt(4)
	v_fmac_f32_e32 v147, v149, v151
	v_exp_f32_e32 v147, v147
	v_add_f32_e32 v146, 1.0, v146
	v_mfma_f32_16x16x32_f16 v[152:155], v[26:29], v[220:223], v[152:155]
	v_rcp_f32_e32 v146, v146
	v_add_f32_e32 v147, 1.0, v147
	v_rcp_f32_e32 v148, v148
	v_mfma_f32_16x16x32_f16 v[182:185], v[34:37], v[220:223], v[166:169]
	v_add_f32_e32 v150, 1.0, v150
	v_rcp_f32_e32 v147, v147
	v_rcp_f32_e32 v150, v150
	v_mfma_f32_16x16x32_f16 v[174:177], v[78:81], v[220:223], v[178:181]
	ds_read_b128 v[166:169], v199 offset:0x3000
	s_waitcnt lgkmcnt(4)
	v_fma_f32 v146, v146, -2.0, 1.0
	v_mfma_f32_16x16x32_f16 v[152:155], v[30:33], v[224:227], v[152:155]
	v_fma_f32 v146, -v148, v146, v146
	v_fma_f32 v151, v147, -2.0, 1.0
	v_fma_mixlo_f16 v189, v148, v1, v146 op_sel_hi:[0,1,0]
	v_mfma_f32_16x16x32_f16 v[178:181], v[38:41], v[224:227], v[182:185]
	v_fma_f32 v151, -v150, v151, v151
	ds_read_b128 v[158:161], v200 offset:0x3000
	s_waitcnt lgkmcnt(4)
	v_mfma_f32_16x16x32_f16 v[174:177], v[82:85], v[224:227], v[174:177]
	v_fma_mixhi_f16 v189, v150, v1, v151 op_sel:[0,1,0] op_sel_hi:[0,1,0]
	global_store_dwordx2 v219, v[188:189], s[0:1] nt
	v_mfma_f32_16x16x32_f16 v[154:157], v[54:57], v[170:173], v[152:155]
	v_mfma_f32_16x16x32_f16 v[146:149], v[62:65], v[170:173], v[178:181]
	v_mfma_f32_16x16x32_f16 v[150:153], v[94:97], v[170:173], v[174:177]
	ds_read_b64 v[188:189], v204 offset:0x2000
	ds_read_b64 v[0:1], v204 offset:0x3000
	ds_read_b128 v[170:173], v206 offset:0x3000
	s_waitcnt lgkmcnt(6)
	s_waitcnt vmcnt(2)
	s_nop 0
	v_mfma_f32_16x16x32_f16 v[182:185], v[2:5], v[228:231], v[118:121]
	v_mfma_f32_16x16x32_f16 v[174:177], v[42:45], v[228:231], v[122:125]
	v_mfma_f32_16x16x32_f16 v[178:181], v[66:69], v[228:231], v[126:129]
	s_and_saveexec_b64 s[2:3], s[6:7]
	s_cbranch_execz .LBB6_13
	s_xor_b32 s23, s23, 0x1000
	v_cvt_pk_f16_f32 v221, v140, v141
	v_cvt_pk_f16_f32 v220, v138, v139
	v_cvt_pk_f16_f32 v223, v136, v137
	v_cvt_pk_f16_f32 v222, v134, v135
	v_add_u32_e32 v134, s23, v205
	ds_write_b128 v134, v[220:223] offset:49152
	s_branch .LBB6_13
.LBB6_18:
	v_exp_f32_e32 v2, v142
	v_exp_f32_e32 v4, v143
	v_exp_f32_e32 v3, v138
	v_exp_f32_e32 v6, v139
	v_add_f32_e32 v2, 1.0, v2
	v_rcp_f32_e32 v2, v2
	v_add_f32_e32 v4, 1.0, v4
	v_rcp_f32_e32 v4, v4
	v_add_f32_e32 v3, 1.0, v3
	v_fma_f32 v2, v146, v2, v134
	v_exp_f32_e32 v5, v2
	v_fma_f32 v2, v147, v4, v135
	v_exp_f32_e32 v7, v2
	v_rcp_f32_e32 v2, v3
	v_add_f32_e32 v3, 1.0, v5
	v_rcp_f32_e32 v4, v3
	v_add_f32_e32 v3, 1.0, v7
	v_rcp_f32_e32 v5, v3
	v_add_f32_e32 v3, 1.0, v6
	v_rcp_f32_e32 v3, v3
	v_cvt_f32_f16_sdwa v7, v0 dst_sel:DWORD dst_unused:UNUSED_PAD src0_sel:WORD_1
	v_cvt_f32_f16_e32 v6, v0
	v_pk_fma_f32 v[4:5], v[4:5], 2.0, 1.0 op_sel_hi:[1,0,0] neg_lo:[1,0,0] neg_hi:[1,0,0]
	v_exp_f32_e32 v8, v144
	v_pk_fma_f32 v[4:5], v[2:3], v[4:5], v[4:5] neg_lo:[1,0,0] neg_hi:[1,0,0]
	v_cvt_f32_f16_sdwa v9, v1 dst_sel:DWORD dst_unused:UNUSED_PAD src0_sel:WORD_1
	v_pk_fma_f32 v[2:3], v[2:3], v[6:7], v[4:5]
	v_exp_f32_e32 v4, v145
	v_add_f32_e32 v0, 1.0, v8
	v_rcp_f32_e32 v0, v0
	v_exp_f32_e32 v8, v140
	v_add_f32_e32 v4, 1.0, v4
	v_rcp_f32_e32 v6, v4
	v_fma_f32 v0, v148, v0, v136
	v_add_f32_e32 v5, 1.0, v8
	v_exp_f32_e32 v0, v0
	v_rcp_f32_e32 v4, v5
	v_exp_f32_e32 v5, v141
	v_fmac_f32_e32 v137, v149, v6
	v_exp_f32_e32 v7, v137
	v_add_f32_e32 v0, 1.0, v0
	v_rcp_f32_e32 v6, v0
	v_add_f32_e32 v0, 1.0, v5
	v_rcp_f32_e32 v5, v0
	v_add_f32_e32 v0, 1.0, v7
	v_rcp_f32_e32 v7, v0
	v_cvt_f32_f16_e32 v8, v1
	v_cvt_pk_f16_f32 v0, v2, v3
	s_lshl_b32 s2, s22, 14
	v_pk_fma_f32 v[2:3], v[6:7], 2.0, 1.0 op_sel_hi:[1,0,0] neg_lo:[1,0,0] neg_hi:[1,0,0]
	v_or_b32_e32 v10, v191, v193
	v_pk_fma_f32 v[2:3], v[4:5], v[2:3], v[2:3] neg_lo:[1,0,0] neg_hi:[1,0,0]
	s_add_i32 s2, s2, s18
	v_pk_fma_f32 v[2:3], v[4:5], v[8:9], v[2:3]
	s_nop 0
	v_cvt_pk_f16_f32 v1, v2, v3
	v_add_u32_e32 v2, s2, v10
	v_add_u32_e32 v2, 0x3000, v2
	global_store_dwordx2 v2, v[0:1], s[0:1] nt
	s_waitcnt vmcnt(0)
	s_endpgm
	.p2alignl 8, 3212836864
